# stack7_nt_cvnt + sc1 on the non-temporal f32 expert-weight loads of the P2 conversion
# speedup vs baseline: 1.0043x; 1.0043x over previous
; #define G8_STAGE(bufoff, gbase, v0, v1) do { unsigned x0_ = (v0), x1_ = (v1); asm volatile("" : "+v"(x0_), "+v"(x1_));     \
;         __builtin_amdgcn_global_load_lds((const unsigned*)((gbase) + x0_), (LAS unsigned*)(lds + (bufoff) + ldsw), 16, 0, 0); \
;         __builtin_amdgcn_global_load_lds((const unsigned*)((gbase) + x1_), (LAS unsigned*)(lds + (bufoff) + ldsw + 8192), 16, 0, 0); } while (0)
; #define G8_LDA(dst, b, h) do { _Pragma("unroll") for (int m = 0; m < 4; ++m) _Pragma("unroll") for (int k = 0; k < 2; ++k) dst[m][k] = *(const LAS bf16x8*)(lds + G8_SA(b, h) + aoff + m * 2048 + k * 1024); } while (0)
; #define G8_LDB(dst, b, h) do { _Pragma("unroll") for (int n = 0; n < 2; ++n) _Pragma("unroll") for (int k = 0; k < 2; ++k) dst[n][k] = *(const LAS bf16x8*)(lds + G8_SB(b, h) + boff + n * 2048 + k * 1024); } while (0)
; #define G8_WAIT_V(n) asm volatile("s_waitcnt vmcnt(" #n ")" ::: "memory")
; #define G8_WAIT_L(n) asm volatile("s_waitcnt lgkmcnt(" #n ")" ::: "memory")
; #define G8_BAR __builtin_amdgcn_s_barrier()
; #define G8_SCHED __builtin_amdgcn_sched_barrier(0)
;     ...
;             G8_BAR; G8_CONV_ISSUE;
;             G8_WAIT_L(0); if (do0) G8_MMA(0, 1, At, B1); G8_BAR;
;             G8_LDA(At, 0, 1); G8_STAGE(G8_SA(0, 0), a2, o00, o01);
;             G8_BAR; G8_WAIT_L(0); if (do1) G8_MMA(1, 0, At, B0); G8_BAR; G8_SCHED;
;             G8_STAGE(G8_SB(0, 1), b2 + hstepB, voffB[0], voffB[1]);
;             if constexpr (CONV) G8_WAIT_V(9); else G8_WAIT_V(6);
;             G8_BAR; if (do1) G8_MMA(1, 1, At, B1); G8_BAR;
;             G8_LDB(B0, 1, 0); G8_SCHED; G8_LDA(At, 1, 0); G8_STAGE(G8_SA(0, 1), a2, o10, o11);
.LBB0_241:
	s_add_u32 s40, s42, 0x8000
	s_addc_u32 s41, s43, 0
	s_and_b32 s49, s62, 3
	s_lshl_b32 s4, s49, 7
	s_add_u32 s4, s28, s4
	v_lshrrev_b32_e32 v212, 3, v194
	v_lshlrev_b32_e32 v194, 4, v194
	s_addc_u32 s5, s29, 0
	s_mul_i32 s64, s14, s8
	v_and_b32_e32 v194, 0x70, v194
	s_mul_hi_u32 s62, s14, s8
	s_add_u32 s4, s4, s64
	v_mad_u64_u32 v[212:213], vcc, s14, v212, v[194:195]
	s_addc_u32 s5, s5, s62
	s_add_i32 m0, s50, 0x20000
	s_lshl_b64 vcc, s[14:15], 6
	global_load_lds_dwordx4 v212, s[4:5] sc1 nt
	s_add_u32 s4, s4, vcc_lo
	s_addc_u32 s5, s5, vcc_hi
	s_mov_b32 m0, s24
	s_lshl_b32 s49, s49, 12
	global_load_lds_dwordx4 v212, s[4:5] sc1 nt
	s_waitcnt lgkmcnt(0)
	s_setprio 1
	s_waitcnt lgkmcnt(0)
	v_mfma_f32_16x16x32_bf16 v[94:97], v[146:149], v[186:189], v[94:97]
	v_mfma_f32_16x16x32_bf16 v[90:93], v[154:157], v[186:189], v[90:93]
	v_mfma_f32_16x16x32_bf16 v[86:89], v[146:149], v[178:181], v[86:89]
	v_mfma_f32_16x16x32_bf16 v[82:85], v[154:157], v[178:181], v[82:85]
	v_mfma_f32_16x16x32_bf16 v[78:81], v[146:149], v[170:173], v[78:81]
	v_mfma_f32_16x16x32_bf16 v[74:77], v[154:157], v[170:173], v[74:77]
	v_mfma_f32_16x16x32_bf16 v[70:73], v[146:149], v[162:165], v[70:73]
	v_mfma_f32_16x16x32_bf16 v[66:69], v[154:157], v[162:165], v[66:69]
	v_mfma_f32_16x16x32_bf16 v[94:97], v[150:153], v[190:193], v[94:97]
	v_mfma_f32_16x16x32_bf16 v[90:93], v[158:161], v[190:193], v[90:93]
	v_mfma_f32_16x16x32_bf16 v[86:89], v[150:153], v[182:185], v[86:89]
	v_mfma_f32_16x16x32_bf16 v[82:85], v[158:161], v[182:185], v[82:85]
	v_mfma_f32_16x16x32_bf16 v[78:81], v[150:153], v[174:177], v[78:81]
	v_mfma_f32_16x16x32_bf16 v[74:77], v[158:161], v[174:177], v[74:77]
	v_mfma_f32_16x16x32_bf16 v[70:73], v[150:153], v[166:169], v[70:73]
	v_mfma_f32_16x16x32_bf16 v[66:69], v[158:161], v[166:169], v[66:69]
	s_setprio 0
	v_mov_b32_e32 v194, v202
	v_mov_b32_e32 v212, v201
	s_mov_b32 m0, s78
	s_barrier
	ds_read_b128 v[162:165], v210 offset:16384
	ds_read_b128 v[166:169], v210 offset:17408
	ds_read_b128 v[170:173], v210 offset:18432
	ds_read_b128 v[174:177], v210 offset:19456
	ds_read_b128 v[178:181], v210 offset:20480
	ds_read_b128 v[182:185], v210 offset:21504
	ds_read_b128 v[186:189], v210 offset:22528
	ds_read_b128 v[190:193], v210 offset:23552
	s_nop 0
	global_load_lds_dwordx4 v212, s[46:47]
	s_mov_b32 m0, s79
	s_nop 0
	global_load_lds_dwordx4 v194, s[46:47]
	s_barrier
	s_waitcnt lgkmcnt(0)
	s_setprio 1
	s_waitcnt lgkmcnt(0)
	v_mfma_f32_16x16x32_bf16 v[62:65], v[130:133], v[162:165], v[62:65]
	v_mfma_f32_16x16x32_bf16 v[58:61], v[138:141], v[162:165], v[58:61]
	v_mfma_f32_16x16x32_bf16 v[54:57], v[130:133], v[170:173], v[54:57]
	v_mfma_f32_16x16x32_bf16 v[50:53], v[138:141], v[170:173], v[50:53]
	v_mfma_f32_16x16x32_bf16 v[38:41], v[130:133], v[178:181], v[38:41]
	v_mfma_f32_16x16x32_bf16 v[34:37], v[138:141], v[178:181], v[34:37]
	v_mfma_f32_16x16x32_bf16 v[22:25], v[130:133], v[186:189], v[22:25]
	v_mfma_f32_16x16x32_bf16 v[18:21], v[138:141], v[186:189], v[18:21]
	v_mfma_f32_16x16x32_bf16 v[62:65], v[134:137], v[166:169], v[62:65]
	v_mfma_f32_16x16x32_bf16 v[58:61], v[142:145], v[166:169], v[58:61]
	v_mfma_f32_16x16x32_bf16 v[54:57], v[134:137], v[174:177], v[54:57]
	v_mfma_f32_16x16x32_bf16 v[50:53], v[142:145], v[174:177], v[50:53]
	v_mfma_f32_16x16x32_bf16 v[38:41], v[134:137], v[182:185], v[38:41]
	v_mfma_f32_16x16x32_bf16 v[34:37], v[142:145], v[182:185], v[34:37]
	v_mfma_f32_16x16x32_bf16 v[22:25], v[134:137], v[190:193], v[22:25]
	v_mfma_f32_16x16x32_bf16 v[18:21], v[142:145], v[190:193], v[18:21]
	s_setprio 0
	s_barrier
	s_add_u32 s4, s42, 0x4000
	v_mov_b32_e32 v130, v1
	v_mov_b32_e32 v131, v198
	s_addc_u32 s5, s43, 0
	s_mov_b32 m0, s80
	s_nop 0
	global_load_lds_dwordx4 v130, s[4:5]
	s_mov_b32 m0, s81
	s_nop 0
	global_load_lds_dwordx4 v131, s[4:5]
	s_waitcnt vmcnt(9)
	s_barrier
	s_setprio 1
	v_mfma_f32_16x16x32_bf16 v[46:49], v[146:149], v[162:165], v[46:49]
	v_mfma_f32_16x16x32_bf16 v[42:45], v[154:157], v[162:165], v[42:45]
	v_mfma_f32_16x16x32_bf16 v[30:33], v[146:149], v[170:173], v[30:33]
	v_mfma_f32_16x16x32_bf16 v[26:29], v[154:157], v[170:173], v[26:29]
	v_mfma_f32_16x16x32_bf16 v[14:17], v[146:149], v[178:181], v[14:17]
	v_mfma_f32_16x16x32_bf16 v[10:13], v[154:157], v[178:181], v[10:13]
	v_mfma_f32_16x16x32_bf16 v[6:9], v[146:149], v[186:189], v[6:9]
	v_mfma_f32_16x16x32_bf16 v[2:5], v[154:157], v[186:189], v[2:5]
	v_mfma_f32_16x16x32_bf16 v[46:49], v[150:153], v[166:169], v[46:49]
	v_mfma_f32_16x16x32_bf16 v[42:45], v[158:161], v[166:169], v[42:45]
	v_mfma_f32_16x16x32_bf16 v[30:33], v[150:153], v[174:177], v[30:33]
	v_mfma_f32_16x16x32_bf16 v[26:29], v[158:161], v[174:177], v[26:29]
	v_mfma_f32_16x16x32_bf16 v[14:17], v[150:153], v[182:185], v[14:17]
	v_mfma_f32_16x16x32_bf16 v[10:13], v[158:161], v[182:185], v[10:13]
	v_mfma_f32_16x16x32_bf16 v[6:9], v[150:153], v[190:193], v[6:9]
	v_mfma_f32_16x16x32_bf16 v[2:5], v[158:161], v[190:193], v[2:5]
	s_setprio 0
	s_add_i32 s4, 0, 0x18000
	v_add_u32_e32 v142, s4, v209
	s_barrier
	ds_read_b128 v[130:133], v142
	ds_read_b128 v[134:137], v142 offset:1024
	ds_read_b128 v[138:141], v142 offset:2048
	ds_read_b128 v[142:145], v142 offset:3072
	v_mov_b32_e32 v178, v203
	v_mov_b32_e32 v179, v204
	s_mov_b32 m0, s82
	ds_read_b128 v[146:149], v210 offset:32768
	ds_read_b128 v[150:153], v210 offset:33792
	ds_read_b128 v[154:157], v210 offset:34816
	ds_read_b128 v[158:161], v210 offset:35840
	ds_read_b128 v[162:165], v210 offset:36864
	ds_read_b128 v[166:169], v210 offset:37888
	ds_read_b128 v[170:173], v210 offset:38912
	ds_read_b128 v[174:177], v210 offset:39936
	s_nop 0
	global_load_lds_dwordx4 v178, s[46:47]
	s_mov_b32 m0, s83
	s_nop 0
	global_load_lds_dwordx4 v179, s[46:47]
	s_waitcnt lgkmcnt(8)
	s_barrier
; #define G8_STAGE(bufoff, gbase, v0, v1) do { unsigned x0_ = (v0), x1_ = (v1); asm volatile("" : "+v"(x0_), "+v"(x1_));     \
;         __builtin_amdgcn_global_load_lds((const unsigned*)((gbase) + x0_), (LAS unsigned*)(lds + (bufoff) + ldsw), 16, 0, 0); \
;         __builtin_amdgcn_global_load_lds((const unsigned*)((gbase) + x1_), (LAS unsigned*)(lds + (bufoff) + ldsw + 8192), 16, 0, 0); } while (0)
; #define G8_LDA(dst, b, h) do { _Pragma("unroll") for (int m = 0; m < 4; ++m) _Pragma("unroll") for (int k = 0; k < 2; ++k) dst[m][k] = *(const LAS bf16x8*)(lds + G8_SA(b, h) + aoff + m * 2048 + k * 1024); } while (0)
; #define G8_LDB(dst, b, h) do { _Pragma("unroll") for (int n = 0; n < 2; ++n) _Pragma("unroll") for (int k = 0; k < 2; ++k) dst[n][k] = *(const LAS bf16x8*)(lds + G8_SB(b, h) + boff + n * 2048 + k * 1024); } while (0)
; #define G8_WAIT_V(n) asm volatile("s_waitcnt vmcnt(" #n ")" ::: "memory")
; #define G8_WAIT_L(n) asm volatile("s_waitcnt lgkmcnt(" #n ")" ::: "memory")
; #define G8_BAR __builtin_amdgcn_s_barrier()
; #define G8_SCHED __builtin_amdgcn_sched_barrier(0)
;     ...
;             G8_LDB(B0, 1, 0); G8_SCHED; G8_LDA(At, 1, 0); G8_STAGE(G8_SA(0, 1), a2, o10, o11);
;             G8_WAIT_L(8); G8_BAR; G8_WAIT_L(0); if (do0) G8_MMA(0, 0, At, B0); G8_BAR; G8_SCHED;
;             G8_LDB(B1, 1, 1); G8_STAGE(G8_SB(1, 0), b3, voffB[0], voffB[1]);
;             G8_BAR; G8_WAIT_L(0); if (do0) G8_MMA(0, 1, At, B1); G8_BAR;
;             G8_LDA(At, 1, 1); G8_STAGE(G8_SA(1, 0), a3, o00, o01);
;             G8_BAR; G8_WAIT_L(0); if (do1) G8_MMA(1, 0, At, B0); G8_BAR; G8_SCHED;
;             G8_STAGE(G8_SB(1, 1), b3 + hstepB, voffB[0], voffB[1]);
;             G8_WAIT_V(6); G8_BAR; if (do1) G8_MMA(1, 1, At, B1); G8_BAR;
;         }
	s_waitcnt lgkmcnt(0)
	s_setprio 1
	s_waitcnt lgkmcnt(0)
	v_mfma_f32_16x16x32_bf16 v[126:129], v[130:133], v[146:149], v[126:129]
	v_mfma_f32_16x16x32_bf16 v[122:125], v[138:141], v[146:149], v[122:125]
	v_mfma_f32_16x16x32_bf16 v[118:121], v[130:133], v[154:157], v[118:121]
	v_mfma_f32_16x16x32_bf16 v[114:117], v[138:141], v[154:157], v[114:117]
	v_mfma_f32_16x16x32_bf16 v[110:113], v[130:133], v[162:165], v[110:113]
	v_mfma_f32_16x16x32_bf16 v[106:109], v[138:141], v[162:165], v[106:109]
	v_mfma_f32_16x16x32_bf16 v[102:105], v[130:133], v[170:173], v[102:105]
	v_mfma_f32_16x16x32_bf16 v[98:101], v[138:141], v[170:173], v[98:101]
	v_mfma_f32_16x16x32_bf16 v[126:129], v[134:137], v[150:153], v[126:129]
	v_mfma_f32_16x16x32_bf16 v[122:125], v[142:145], v[150:153], v[122:125]
	v_mfma_f32_16x16x32_bf16 v[118:121], v[134:137], v[158:161], v[118:121]
	v_mfma_f32_16x16x32_bf16 v[114:117], v[142:145], v[158:161], v[114:117]
	v_mfma_f32_16x16x32_bf16 v[110:113], v[134:137], v[166:169], v[110:113]
	v_mfma_f32_16x16x32_bf16 v[106:109], v[142:145], v[166:169], v[106:109]
	v_mfma_f32_16x16x32_bf16 v[102:105], v[134:137], v[174:177], v[102:105]
	v_mfma_f32_16x16x32_bf16 v[98:101], v[142:145], v[174:177], v[98:101]
	s_setprio 0
	s_barrier
	s_add_i32 s62, 0, 0x1c000
	s_add_i32 s4, s4, s77
	v_add_u32_e32 v190, s62, v209
	v_mov_b32_e32 v194, v1
	v_mov_b32_e32 v212, v198
	s_mov_b32 m0, s4
	ds_read_b128 v[178:181], v190
	ds_read_b128 v[182:185], v190 offset:1024
	ds_read_b128 v[186:189], v190 offset:2048
	ds_read_b128 v[190:193], v190 offset:3072
	s_nop 0
	global_load_lds_dwordx4 v194, s[40:41]
	s_add_i32 m0, s4, 0x2000
	s_nop 0
	global_load_lds_dwordx4 v212, s[40:41]
	s_barrier
	s_waitcnt lgkmcnt(0)
	s_setprio 1
	s_waitcnt lgkmcnt(0)
	v_mfma_f32_16x16x32_bf16 v[94:97], v[178:181], v[146:149], v[94:97]
	v_mfma_f32_16x16x32_bf16 v[90:93], v[186:189], v[146:149], v[90:93]
	v_mfma_f32_16x16x32_bf16 v[86:89], v[178:181], v[154:157], v[86:89]
	v_mfma_f32_16x16x32_bf16 v[82:85], v[186:189], v[154:157], v[82:85]
	v_mfma_f32_16x16x32_bf16 v[78:81], v[178:181], v[162:165], v[78:81]
	v_mfma_f32_16x16x32_bf16 v[74:77], v[186:189], v[162:165], v[74:77]
	v_mfma_f32_16x16x32_bf16 v[70:73], v[178:181], v[170:173], v[70:73]
	v_mfma_f32_16x16x32_bf16 v[66:69], v[186:189], v[170:173], v[66:69]
	v_mfma_f32_16x16x32_bf16 v[94:97], v[182:185], v[150:153], v[94:97]
	v_mfma_f32_16x16x32_bf16 v[90:93], v[190:193], v[150:153], v[90:93]
	v_mfma_f32_16x16x32_bf16 v[86:89], v[182:185], v[158:161], v[86:89]
	v_mfma_f32_16x16x32_bf16 v[82:85], v[190:193], v[158:161], v[82:85]
	v_mfma_f32_16x16x32_bf16 v[78:81], v[182:185], v[166:169], v[78:81]
	v_mfma_f32_16x16x32_bf16 v[74:77], v[190:193], v[166:169], v[74:77]
	v_mfma_f32_16x16x32_bf16 v[70:73], v[182:185], v[174:177], v[70:73]
	v_mfma_f32_16x16x32_bf16 v[66:69], v[190:193], v[174:177], v[66:69]
	s_setprio 0
	v_mov_b32_e32 v212, v202
	v_mov_b32_e32 v194, v201
	s_barrier
	ds_read_b128 v[146:149], v210 offset:49152
	ds_read_b128 v[150:153], v210 offset:50176
	ds_read_b128 v[154:157], v210 offset:51200
	ds_read_b128 v[158:161], v210 offset:52224
	ds_read_b128 v[162:165], v210 offset:53248
	ds_read_b128 v[166:169], v210 offset:54272
	ds_read_b128 v[170:173], v210 offset:55296
	ds_read_b128 v[174:177], v210 offset:56320
	v_mov_b32_e32 v213, v195
	v_lshl_add_u64 v[214:215], s[46:47], 0, v[194:195]
	s_mov_b32 m0, s90
	v_lshl_add_u64 v[214:215], v[214:215], 0, s[26:27]
	v_lshl_add_u64 v[212:213], s[46:47], 0, v[212:213]
	global_load_lds_dwordx4 v[214:215], off
	v_lshl_add_u64 v[212:213], v[212:213], 0, s[26:27]
	s_mov_b32 m0, s91
	s_nop 0
	global_load_lds_dwordx4 v[212:213], off
	s_barrier
	s_waitcnt lgkmcnt(0)
	s_setprio 1
	s_waitcnt lgkmcnt(0)
	v_mfma_f32_16x16x32_bf16 v[62:65], v[130:133], v[146:149], v[62:65]
	v_mfma_f32_16x16x32_bf16 v[58:61], v[138:141], v[146:149], v[58:61]
	v_mfma_f32_16x16x32_bf16 v[54:57], v[130:133], v[154:157], v[54:57]
	v_mfma_f32_16x16x32_bf16 v[50:53], v[138:141], v[154:157], v[50:53]
	v_mfma_f32_16x16x32_bf16 v[38:41], v[130:133], v[162:165], v[38:41]
	v_mfma_f32_16x16x32_bf16 v[34:37], v[138:141], v[162:165], v[34:37]
	v_mfma_f32_16x16x32_bf16 v[22:25], v[130:133], v[170:173], v[22:25]
	v_mfma_f32_16x16x32_bf16 v[18:21], v[138:141], v[170:173], v[18:21]
	v_mfma_f32_16x16x32_bf16 v[62:65], v[134:137], v[150:153], v[62:65]
	v_mfma_f32_16x16x32_bf16 v[58:61], v[142:145], v[150:153], v[58:61]
	v_mfma_f32_16x16x32_bf16 v[54:57], v[134:137], v[158:161], v[54:57]
	v_mfma_f32_16x16x32_bf16 v[50:53], v[142:145], v[158:161], v[50:53]
	v_mfma_f32_16x16x32_bf16 v[38:41], v[134:137], v[166:169], v[38:41]
	v_mfma_f32_16x16x32_bf16 v[34:37], v[142:145], v[166:169], v[34:37]
	v_mfma_f32_16x16x32_bf16 v[22:25], v[134:137], v[174:177], v[22:25]
	v_mfma_f32_16x16x32_bf16 v[18:21], v[142:145], v[174:177], v[18:21]
	s_setprio 0
	s_barrier
	s_add_u32 s4, s42, 0xc000
	s_addc_u32 s5, s43, 0
	s_add_i32 s40, s62, s77
	v_mov_b32_e32 v130, v1
	v_mov_b32_e32 v131, v198
	s_mov_b32 m0, s40
	s_nop 0
	global_load_lds_dwordx4 v130, s[4:5]
	s_add_i32 m0, s40, 0x2000
	s_nop 0
	global_load_lds_dwordx4 v131, s[4:5]
	s_waitcnt vmcnt(6)
	s_barrier
	s_setprio 1
	v_mfma_f32_16x16x32_bf16 v[46:49], v[178:181], v[146:149], v[46:49]
	s_add_u32 s40, s30, s49
	s_addc_u32 s41, s31, 0
	v_mfma_f32_16x16x32_bf16 v[42:45], v[186:189], v[146:149], v[42:45]
	v_mfma_f32_16x16x32_bf16 v[30:33], v[178:181], v[154:157], v[30:33]
	v_mfma_f32_16x16x32_bf16 v[26:29], v[186:189], v[154:157], v[26:29]
	v_mfma_f32_16x16x32_bf16 v[14:17], v[178:181], v[162:165], v[14:17]
	v_mfma_f32_16x16x32_bf16 v[10:13], v[186:189], v[162:165], v[10:13]
	v_mfma_f32_16x16x32_bf16 v[6:9], v[178:181], v[170:173], v[6:9]
	v_mfma_f32_16x16x32_bf16 v[2:5], v[186:189], v[170:173], v[2:5]
	v_mfma_f32_16x16x32_bf16 v[46:49], v[182:185], v[150:153], v[46:49]
	v_mfma_f32_16x16x32_bf16 v[42:45], v[190:193], v[150:153], v[42:45]
	v_mfma_f32_16x16x32_bf16 v[30:33], v[182:185], v[158:161], v[30:33]
	v_mfma_f32_16x16x32_bf16 v[26:29], v[190:193], v[158:161], v[26:29]
	v_mfma_f32_16x16x32_bf16 v[14:17], v[182:185], v[166:169], v[14:17]
	v_mfma_f32_16x16x32_bf16 v[10:13], v[190:193], v[166:169], v[10:13]
	v_mfma_f32_16x16x32_bf16 v[6:9], v[182:185], v[174:177], v[6:9]
	v_mfma_f32_16x16x32_bf16 v[2:5], v[190:193], v[174:177], v[2:5]
	s_setprio 0
	s_add_i32 s61, s61, 2
	s_add_u32 s6, s6, 0x10000
	s_addc_u32 s7, s7, 0
	s_add_u32 s0, s0, 0x100
	s_addc_u32 s1, s1, 0
	s_add_i32 s49, s68, 1
	s_cmp_gt_u32 s61, 29
	s_barrier
	s_cbranch_scc1 .LBB0_243
	s_mov_b32 s68, s49
	s_branch .LBB0_234

; __device__ __forceinline__ void cvt8_load(const Cvt8Unit& u, int tid, f32x4 (&r)[8]) {
;     const int kg = tid >> 5, nq = tid & 31;
;     const float* p = u.src + (size_t)(u.k0 + 8 * kg) * u.Nd + u.n0 + nq * 4;
; #pragma unroll
;     for (int kk = 0; kk < 8; ++kk) r[kk] = __builtin_nontemporal_load((const f32x4*)(p + (size_t)kk * u.Nd));
; }
; __device__ __forceinline__ void p0_convert_fp8(const Params& P, LAS unsigned char* lds, int tid, int blk, int G, const int Lbeg, const int Lend) {
;     ...
;     int L = Lbeg + blk;
;     if (L >= Lend) return;
;     bool hasB = (L + G) < Lend;
;     cvt8_decode(P, L, uA); cvt8_load(uA, tid, rA);
;     if (hasB) { cvt8_decode(P, L + G, uB); cvt8_load(uB, tid, rB); }
.LBB0_293:
	v_ashrrev_i32_e32 v134, 2, v66
	s_add_i32 s29, s29, s33
	v_and_b32_e32 v135, -8, v134
	s_cmpk_lt_i32 s29, 0x2d00
	v_add_u32_e32 v2, s8, v135
	s_cselect_b64 s[30:31], -1, 0
	s_lshl_b32 s34, s6, 2
	v_mad_i64_i32 v[2:3], s[6:7], s6, v2, 0
	v_lshlrev_b32_e32 v4, 2, v66
	v_lshl_add_u64 v[2:3], v[2:3], 2, s[4:5]
	v_and_b32_e32 v4, 0x7c, v4
	v_lshl_add_u64 v[2:3], s[14:15], 2, v[2:3]
	v_lshlrev_b32_e32 v130, 2, v4
	v_mov_b32_e32 v131, v195
	v_lshl_add_u64 v[2:3], v[2:3], 0, v[130:131]
	s_mov_b32 s35, s15
	v_lshl_add_u64 v[4:5], v[2:3], 0, s[34:35]
	global_load_dwordx4 v[62:65], v[2:3], off sc1 nt
	global_load_dwordx4 v[58:61], v[4:5], off sc1 nt
	v_lshl_add_u64 v[2:3], v[4:5], 0, s[34:35]
	v_lshl_add_u64 v[4:5], v[2:3], 0, s[34:35]
	global_load_dwordx4 v[54:57], v[2:3], off sc1 nt
	global_load_dwordx4 v[50:53], v[4:5], off sc1 nt
	v_lshl_add_u64 v[2:3], v[4:5], 0, s[34:35]
	v_lshl_add_u64 v[4:5], v[2:3], 0, s[34:35]
	global_load_dwordx4 v[46:49], v[2:3], off sc1 nt
	global_load_dwordx4 v[42:45], v[4:5], off sc1 nt
	v_lshl_add_u64 v[2:3], v[4:5], 0, s[34:35]
	v_lshl_add_u64 v[4:5], v[2:3], 0, s[34:35]
	global_load_dwordx4 v[38:41], v[2:3], off sc1 nt
	global_load_dwordx4 v[30:33], v[4:5], off sc1 nt
	s_cmpk_gt_i32 s29, 0x2cff
	s_cbranch_scc1 .LBB0_300
	s_cmpk_gt_i32 s29, 0x1fff
	s_mov_b64 s[34:35], -1
	s_cbranch_scc0 .LBB0_296
	s_add_i32 s4, s29, 0xffffe000
	s_lshr_b32 s4, s4, 7
	s_mov_b32 s5, s15
	s_lshl_b64 s[6:7], s[4:5], 23
	s_add_u32 s6, s18, s6
	s_addc_u32 s7, s19, s7
	s_lshl_b64 s[4:5], s[4:5], 21
	s_add_u32 s4, s53, s4
	s_addc_u32 s5, s54, s5
	s_lshl_b32 s28, s29, 3
	s_and_b32 s44, s28, 0x380
	s_lshl_b32 s28, s29, 7
	s_and_b32 s28, s28, 0x780
	s_mov_b64 s[34:35], 0

; __device__ __forceinline__ void cvt8_load(const Cvt8Unit& u, int tid, f32x4 (&r)[8]) {
;     const int kg = tid >> 5, nq = tid & 31;
;     const float* p = u.src + (size_t)(u.k0 + 8 * kg) * u.Nd + u.n0 + nq * 4;
; #pragma unroll
;     for (int kk = 0; kk < 8; ++kk) r[kk] = __builtin_nontemporal_load((const f32x4*)(p + (size_t)kk * u.Nd));
; }
.LBB0_299:
	v_add_u32_e32 v2, s44, v135
	v_mad_i64_i32 v[2:3], s[36:37], s34, v2, 0
	v_lshl_add_u64 v[2:3], v[2:3], 2, s[6:7]
	s_mov_b32 s29, s15
	v_lshl_add_u64 v[2:3], s[28:29], 2, v[2:3]
	v_mov_b32_e32 v131, v195
	v_lshl_add_u64 v[2:3], v[2:3], 0, v[130:131]
	s_lshl_b32 s6, s34, 2
	s_mov_b32 s7, s15
	v_lshl_add_u64 v[10:11], v[2:3], 0, s[6:7]
	global_load_dwordx4 v[2:5], v[2:3], off sc1 nt
	s_nop 0
	global_load_dwordx4 v[6:9], v[10:11], off sc1 nt
	v_lshl_add_u64 v[10:11], v[10:11], 0, s[6:7]
	v_lshl_add_u64 v[18:19], v[10:11], 0, s[6:7]
	global_load_dwordx4 v[10:13], v[10:11], off sc1 nt
	s_nop 0
	global_load_dwordx4 v[14:17], v[18:19], off sc1 nt
	v_lshl_add_u64 v[18:19], v[18:19], 0, s[6:7]
	v_lshl_add_u64 v[26:27], v[18:19], 0, s[6:7]
	global_load_dwordx4 v[18:21], v[18:19], off sc1 nt
	s_nop 0
	global_load_dwordx4 v[22:25], v[26:27], off sc1 nt
	v_lshl_add_u64 v[26:27], v[26:27], 0, s[6:7]
	v_lshl_add_u64 v[34:35], v[26:27], 0, s[6:7]
	global_load_dwordx4 v[26:29], v[26:27], off sc1 nt
	s_nop 0
	global_load_dwordx4 v[34:37], v[34:35], off sc1 nt

; __device__ __forceinline__ void cvt8_load(const Cvt8Unit& u, int tid, f32x4 (&r)[8]) {
;     const int kg = tid >> 5, nq = tid & 31;
;     const float* p = u.src + (size_t)(u.k0 + 8 * kg) * u.Nd + u.n0 + nq * 4;
; #pragma unroll
;     for (int kk = 0; kk < 8; ++kk) r[kk] = __builtin_nontemporal_load((const f32x4*)(p + (size_t)kk * u.Nd));
; }
; __device__ __forceinline__ void p0_convert_fp8(const Params& P, LAS unsigned char* lds, int tid, int blk, int G, const int Lbeg, const int Lend) {
;     ...
;         const int Ln = L + 2 * G; const bool moreA = Ln < Lend, moreB = (Ln + G) < Lend;
;         if (moreA) { cvt8_decode(P, Ln, nA); cvt8_load(nA, tid, qA); }
;         if (moreB) { cvt8_decode(P, Ln + G, nB); cvt8_load(nB, tid, qB); }
.LBB0_308:
	v_add_u32_e32 v66, s8, v135
	v_mad_i64_i32 v[66:67], s[74:75], s30, v66, 0
	v_lshl_add_u64 v[66:67], v[66:67], 2, s[6:7]
	v_lshl_add_u64 v[66:67], s[14:15], 2, v[66:67]
	v_mov_b32_e32 v131, v195
	v_lshl_add_u64 v[66:67], v[66:67], 0, v[130:131]
	s_lshl_b32 s6, s30, 2
	s_mov_b32 s7, s15
	v_lshl_add_u64 v[74:75], v[66:67], 0, s[6:7]
	global_load_dwordx4 v[70:73], v[66:67], off sc1 nt
	s_nop 0
	global_load_dwordx4 v[66:69], v[74:75], off sc1 nt
	v_lshl_add_u64 v[74:75], v[74:75], 0, s[6:7]
	v_lshl_add_u64 v[82:83], v[74:75], 0, s[6:7]
	global_load_dwordx4 v[78:81], v[74:75], off sc1 nt
	s_nop 0
	global_load_dwordx4 v[74:77], v[82:83], off sc1 nt
	v_lshl_add_u64 v[82:83], v[82:83], 0, s[6:7]
	v_lshl_add_u64 v[90:91], v[82:83], 0, s[6:7]
	global_load_dwordx4 v[86:89], v[82:83], off sc1 nt
	s_nop 0
	global_load_dwordx4 v[82:85], v[90:91], off sc1 nt
	v_lshl_add_u64 v[90:91], v[90:91], 0, s[6:7]
	v_lshl_add_u64 v[92:93], v[90:91], 0, s[6:7]
	global_load_dwordx4 v[94:97], v[90:91], off sc1 nt
	s_nop 0
	global_load_dwordx4 v[90:93], v[92:93], off sc1 nt

; __device__ __forceinline__ void cvt8_load(const Cvt8Unit& u, int tid, f32x4 (&r)[8]) {
;     const int kg = tid >> 5, nq = tid & 31;
;     const float* p = u.src + (size_t)(u.k0 + 8 * kg) * u.Nd + u.n0 + nq * 4;
; #pragma unroll
;     for (int kk = 0; kk < 8; ++kk) r[kk] = __builtin_nontemporal_load((const f32x4*)(p + (size_t)kk * u.Nd));
; }
; __device__ __forceinline__ void p0_convert_fp8(const Params& P, LAS unsigned char* lds, int tid, int blk, int G, const int Lbeg, const int Lend) {
;     ...
;         if (moreB) { cvt8_decode(P, Ln + G, nB); cvt8_load(nB, tid, qB); }
.LBB0_315:
	v_add_u32_e32 v2, s44, v135
	v_mad_i64_i32 v[2:3], s[74:75], s48, v2, 0
	v_lshl_add_u64 v[2:3], v[2:3], 2, s[6:7]
	s_mov_b32 s29, s15
	v_lshl_add_u64 v[2:3], s[28:29], 2, v[2:3]
	v_mov_b32_e32 v131, v195
	v_lshl_add_u64 v[2:3], v[2:3], 0, v[130:131]
	s_lshl_b32 s6, s48, 2
	s_mov_b32 s7, s15
	v_lshl_add_u64 v[10:11], v[2:3], 0, s[6:7]
	global_load_dwordx4 v[2:5], v[2:3], off sc1 nt
	s_nop 0
	global_load_dwordx4 v[6:9], v[10:11], off sc1 nt
	v_lshl_add_u64 v[10:11], v[10:11], 0, s[6:7]
	v_lshl_add_u64 v[18:19], v[10:11], 0, s[6:7]
	global_load_dwordx4 v[10:13], v[10:11], off sc1 nt
	s_nop 0
	global_load_dwordx4 v[14:17], v[18:19], off sc1 nt
	v_lshl_add_u64 v[18:19], v[18:19], 0, s[6:7]
	v_lshl_add_u64 v[26:27], v[18:19], 0, s[6:7]
	global_load_dwordx4 v[18:21], v[18:19], off sc1 nt
	s_nop 0
	global_load_dwordx4 v[22:25], v[26:27], off sc1 nt
	v_lshl_add_u64 v[26:27], v[26:27], 0, s[6:7]
	v_lshl_add_u64 v[34:35], v[26:27], 0, s[6:7]
	global_load_dwordx4 v[26:29], v[26:27], off sc1 nt
	s_nop 0
	global_load_dwordx4 v[34:37], v[34:35], off sc1 nt
